# P7 and P8 expert-GEMM epilogues: all bias loads issued together at epilogue start (P7: before the align barrier) instead of a second dependent round trip behind the first half's stores
# speedup vs baseline: 1.0020x; 1.0020x over previous
; __device__ __forceinline__ int fresh_lane() { int l = (int)__builtin_amdgcn_mbcnt_hi(~0u, __builtin_amdgcn_mbcnt_lo(~0u, 0u)); asm volatile("" : "+v"(l)); return l; }
; __device__ __forceinline__ unsigned pk4_fp8(float a, float b, float c, float d) { int p = 0; p = __builtin_amdgcn_cvt_pk_fp8_f32(a, b, p, false); p = __builtin_amdgcn_cvt_pk_fp8_f32(c, d, p, true); return (unsigned)p; }
;     __device__ __forceinline__ float act1(float g, float up1) const { g = fminf(g, 7.f); up1 = fminf(fmaxf(up1, -6.f), 8.f); return g * __builtin_amdgcn_rcpf(1.f + __builtin_amdgcn_exp2f(g * (-1.702f * 1.44269504f))) * up1; }
; #define PG8_BAR __builtin_amdgcn_s_barrier()
;     __device__ __forceinline__ void operator()(const f32x4 (&acc)[2][2][4][2], const Unit& u, int wr, int wc, int fr, int fq) const {
;         const int row0 = poff[u.e] + u.pm * BM + wr * 64 + fr, col0 = u.pn * BM + wc * 32 + 8 * fq;
;         const float* bp = bias + (size_t)u.e * (2 * DFF) + col0;
;         f32x4 bv[2][2];
; #pragma unroll
;         for (int bj = 0; bj < 2; ++bj)
; #pragma unroll
;             for (int n = 0; n < 2; ++n) { bv[bj][n] = *(const f32x4*)(bp + bj * HALF + 4 * n); bv[bj][n].y += 1.f; bv[bj][n].w += 1.f; }
; #pragma unroll
;         for (int ai = 0; ai < 2; ++ai)
; #pragma unroll
;             for (int m = 0; m < 4; ++m) { unsigned char* rowp = ACT + (size_t)(row0 + ai * HALF + m * 16) * DFF + (col0 >> 1);
; #pragma unroll
;                 for (int bj = 0; bj < 2; ++bj) { const f32x4 v0 = acc[ai][bj][m][0] * WINV + bv[bj][0], v1 = acc[ai][bj][m][1] * WINV + bv[bj][1];
;                     *(unsigned*)(rowp + bj * (HALF / 2)) = pk4_fp8(act1(v0[0], v0[1]), act1(v0[2], v0[3]), act1(v1[0], v1[1]), act1(v1[2], v1[3])); } }
; template <class Epi, class Sched>
; __device__ __forceinline__ void gemm_phase(LAS unsigned char* lds, const Sched& S, const Epi& E) {
;     ...
;         if (wr == 0) PG8_BAR;
;         { const int l2 = fresh_lane(); E(acc, cur, wr, wc, l2 & 15, l2 >> 4); }
.LBB0_1013:
	s_lshl_b32 s12, s52, 2
	s_add_i32 s12, s12, 0
	s_add_i32 s12, s12, 0x20300
	v_mov_b32_e32 v28, v1
	v_mov_b32_e32 v2, s12
	ds_read_b32 v29, v2
	s_lshl_b32 s12, s54, 8
	v_ashrrev_i32_e32 v2, 1, v28
	s_ashr_i32 s53, s52, 31
	v_and_b32_e32 v2, -8, v2
	s_or_b32 s12, s12, s22
	s_lshl_b32 s41, s79, 8
	v_add_u32_e32 v18, s12, v2
	s_lshl_b64 s[12:13], s[52:53], 14
	s_add_u32 s12, s48, s12
	s_addc_u32 s13, s49, s13
	v_ashrrev_i32_e32 v19, 31, v18
	v_lshl_add_u64 v[6:7], v[18:19], 2, s[12:13]
	global_load_dwordx4 v[10:13], v[6:7], off offset:16
	global_load_dwordx4 v[14:17], v[6:7], off
	global_load_dwordx4 v[2:5], v[6:7], off offset:528
	s_nop 0
	global_load_dwordx4 v[6:9], v[6:7], off offset:512
	s_and_b64 vcc, exec, s[4:5]
	s_cbranch_vccz .LBB0_1015
	s_barrier
.LBB0_1015:
	s_add_i32 s41, s41, s94
	v_ashrrev_i32_e32 v18, 1, v18
	v_ashrrev_i32_e32 v19, 31, v18
	v_lshl_add_u64 v[18:19], s[20:21], 0, v[18:19]
	s_mov_b64 s[12:13], 0x8000
	s_mov_b64 s[52:53], -1
	s_waitcnt vmcnt(0)
	v_mov_b32_e32 v20, v15
	v_mov_b32_e32 v21, v17
	v_pk_add_f32 v[24:25], v[20:21], 1.0 op_sel_hi:[1,0]
	v_mov_b32_e32 v20, v11
	v_mov_b32_e32 v21, v13
	v_pk_add_f32 v[26:27], v[20:21], 1.0 op_sel_hi:[1,0]
	v_mov_b32_e32 v15, v24
	v_mov_b32_e32 v17, v25
	v_pk_fma_f32 v[24:25], v[190:191], s[38:39], v[14:15] op_sel_hi:[1,0,1]
	v_mov_b32_e32 v11, v26
	v_mov_b32_e32 v13, v27
	v_pk_fma_f32 v[26:27], v[186:187], s[38:39], v[10:11] op_sel_hi:[1,0,1]
	v_pk_fma_f32 v[30:31], v[188:189], s[38:39], v[12:13] op_sel_hi:[1,0,1]
	s_waitcnt vmcnt(0)
	v_mov_b32_e32 v20, v7
	v_mov_b32_e32 v21, v9
	v_pk_add_f32 v[22:23], v[20:21], 1.0 op_sel_hi:[1,0]
	v_mov_b32_e32 v20, v3
	v_and_or_b32 v3, v28, 15, s41
	s_waitcnt lgkmcnt(0)
	v_add_u32_e32 v28, v3, v29
	v_min_f32_e32 v3, 0x40e00000, v24
	v_mul_f32_e32 v7, 0xc01d265f, v3
	v_exp_f32_e32 v7, v7
	v_ashrrev_i32_e32 v29, 31, v28
	v_lshlrev_b64 v[28:29], 11, v[28:29]
	v_mov_b32_e32 v21, v5
	v_add_f32_e32 v7, 1.0, v7
	v_rcp_f32_e32 v7, v7
	v_lshl_add_u64 v[18:19], v[18:19], 0, v[28:29]
	v_pk_fma_f32 v[28:29], v[192:193], s[38:39], v[16:17] op_sel_hi:[1,0,1]
	v_med3_f32 v5, v25, s23, v200
	v_mul_f32_e32 v3, v3, v7
	v_mul_f32_e32 v3, v5, v3
	v_min_f32_e32 v5, 0x40e00000, v28
	v_mul_f32_e32 v9, 0xc01d265f, v5
	v_exp_f32_e32 v9, v9
	v_med3_f32 v7, v29, s23, v200
	v_pk_add_f32 v[20:21], v[20:21], 1.0 op_sel_hi:[1,0]
	v_add_f32_e32 v9, 1.0, v9
	v_rcp_f32_e32 v9, v9
	s_nop 0
	v_mul_f32_e32 v5, v5, v9
	v_mul_f32_e32 v5, v7, v5
	v_min_f32_e32 v7, 0x40e00000, v26
	v_mul_f32_e32 v24, 0xc01d265f, v7
	v_exp_f32_e32 v24, v24
	v_med3_f32 v9, v27, s23, v200
	v_add_f32_e32 v24, 1.0, v24
	v_rcp_f32_e32 v24, v24
	s_nop 0
	v_mul_f32_e32 v7, v7, v24
	v_mul_f32_e32 v7, v9, v7
	v_min_f32_e32 v9, 0x40e00000, v30
	v_mul_f32_e32 v25, 0xc01d265f, v9
	v_exp_f32_e32 v25, v25
	v_med3_f32 v24, v31, s23, v200
	v_add_f32_e32 v25, 1.0, v25
	v_rcp_f32_e32 v25, v25
	s_nop 0
	v_mul_f32_e32 v9, v9, v25
	v_mul_f32_e32 v9, v24, v9
	v_mov_b32_e32 v24, v195
	v_cvt_pk_fp8_f32 v24, v3, v5
	v_mov_b32_e32 v3, v20
	v_mov_b32_e32 v5, v21
	v_pk_fma_f32 v[20:21], v[178:179], s[38:39], v[2:3] op_sel_hi:[1,0,1]
	v_cvt_pk_fp8_f32 v24, v7, v9 op_sel:[0,0,1]
	v_mov_b32_e32 v7, v22
	v_pk_fma_f32 v[26:27], v[182:183], s[38:39], v[6:7] op_sel_hi:[1,0,1]
	v_mov_b32_e32 v9, v23
	v_min_f32_e32 v26, 0x40e00000, v26
	v_mul_f32_e32 v28, 0xc01d265f, v26
	v_exp_f32_e32 v28, v28
	global_store_dword v[18:19], v24, off
	v_pk_fma_f32 v[24:25], v[184:185], s[38:39], v[8:9] op_sel_hi:[1,0,1]
	v_med3_f32 v27, v27, s23, v200
	v_add_f32_e32 v28, 1.0, v28
	v_rcp_f32_e32 v28, v28
	v_min_f32_e32 v24, 0x40e00000, v24
	v_med3_f32 v25, v25, s23, v200
	v_min_f32_e32 v20, 0x40e00000, v20
	v_mul_f32_e32 v26, v26, v28
	v_mul_f32_e32 v26, v27, v26
	v_mul_f32_e32 v27, 0xc01d265f, v24
	v_exp_f32_e32 v27, v27
	v_pk_fma_f32 v[22:23], v[180:181], s[38:39], v[4:5] op_sel_hi:[1,0,1]
	v_med3_f32 v21, v21, s23, v200
	v_pk_fma_f32 v[28:29], v[170:171], s[38:39], v[10:11] op_sel_hi:[1,0,1]
	v_add_f32_e32 v27, 1.0, v27
	v_rcp_f32_e32 v27, v27
	s_nop 0
	v_mul_f32_e32 v24, v24, v27
	v_mul_f32_e32 v24, v25, v24
	v_mul_f32_e32 v25, 0xc01d265f, v20
	v_exp_f32_e32 v25, v25
	s_nop 0
	v_add_f32_e32 v25, 1.0, v25
	v_rcp_f32_e32 v25, v25
	s_nop 0
	v_mul_f32_e32 v20, v20, v25
	v_mul_f32_e32 v20, v21, v20
	v_min_f32_e32 v21, 0x40e00000, v22
	v_med3_f32 v22, v23, s23, v200
	v_mul_f32_e32 v23, 0xc01d265f, v21
	v_exp_f32_e32 v23, v23
	s_nop 0
	v_add_f32_e32 v23, 1.0, v23
	v_rcp_f32_e32 v23, v23
	s_nop 0
	v_mul_f32_e32 v21, v21, v23
	v_mul_f32_e32 v21, v22, v21
	v_mov_b32_e32 v22, v195
	v_cvt_pk_fp8_f32 v22, v26, v24
	v_pk_fma_f32 v[24:25], v[174:175], s[38:39], v[14:15] op_sel_hi:[1,0,1]
	v_pk_fma_f32 v[26:27], v[172:173], s[38:39], v[12:13] op_sel_hi:[1,0,1]
	v_min_f32_e32 v24, 0x40e00000, v24
	v_mul_f32_e32 v30, 0xc01d265f, v24
	v_exp_f32_e32 v30, v30
	v_cvt_pk_fp8_f32 v22, v20, v21 op_sel:[0,0,1]
	v_med3_f32 v25, v25, s23, v200
	v_lshl_add_u64 v[20:21], v[18:19], 0, s[12:13]
	v_add_f32_e32 v30, 1.0, v30
	v_rcp_f32_e32 v30, v30
	global_store_dword v[18:19], v22, off offset:64
	v_pk_fma_f32 v[22:23], v[176:177], s[38:39], v[16:17] op_sel_hi:[1,0,1]
	s_mov_b32 s12, 0x8000
	v_mul_f32_e32 v24, v24, v30
	v_min_f32_e32 v22, 0x40e00000, v22
	v_mul_f32_e32 v24, v25, v24
	v_mul_f32_e32 v25, 0xc01d265f, v22
	v_exp_f32_e32 v25, v25
	v_med3_f32 v23, v23, s23, v200
	v_add_f32_e32 v25, 1.0, v25
	v_rcp_f32_e32 v25, v25
	s_nop 0
	v_mul_f32_e32 v22, v22, v25
	v_mul_f32_e32 v22, v23, v22
	v_min_f32_e32 v23, 0x40e00000, v28
	v_mul_f32_e32 v28, 0xc01d265f, v23
	v_exp_f32_e32 v28, v28
	v_med3_f32 v25, v29, s23, v200
	v_add_f32_e32 v28, 1.0, v28
	v_rcp_f32_e32 v28, v28
; __device__ __forceinline__ unsigned pk4_fp8(float a, float b, float c, float d) { int p = 0; p = __builtin_amdgcn_cvt_pk_fp8_f32(a, b, p, false); p = __builtin_amdgcn_cvt_pk_fp8_f32(c, d, p, true); return (unsigned)p; }
;     __device__ __forceinline__ float act1(float g, float up1) const { g = fminf(g, 7.f); up1 = fminf(fmaxf(up1, -6.f), 8.f); return g * __builtin_amdgcn_rcpf(1.f + __builtin_amdgcn_exp2f(g * (-1.702f * 1.44269504f))) * up1; }
;     __device__ __forceinline__ void operator()(const f32x4 (&acc)[2][2][4][2], const Unit& u, int wr, int wc, int fr, int fq) const {
;         const int row0 = poff[u.e] + u.pm * BM + wr * 64 + fr, col0 = u.pn * BM + wc * 32 + 8 * fq;
;         const float* bp = bias + (size_t)u.e * (2 * DFF) + col0;
;         f32x4 bv[2][2];
; #pragma unroll
;         for (int bj = 0; bj < 2; ++bj)
; #pragma unroll
;             for (int n = 0; n < 2; ++n) { bv[bj][n] = *(const f32x4*)(bp + bj * HALF + 4 * n); bv[bj][n].y += 1.f; bv[bj][n].w += 1.f; }
; #pragma unroll
;         for (int ai = 0; ai < 2; ++ai)
; #pragma unroll
;             for (int m = 0; m < 4; ++m) { unsigned char* rowp = ACT + (size_t)(row0 + ai * HALF + m * 16) * DFF + (col0 >> 1);
; #pragma unroll
;                 for (int bj = 0; bj < 2; ++bj) { const f32x4 v0 = acc[ai][bj][m][0] * WINV + bv[bj][0], v1 = acc[ai][bj][m][1] * WINV + bv[bj][1];
;                     *(unsigned*)(rowp + bj * (HALF / 2)) = pk4_fp8(act1(v0[0], v0[1]), act1(v0[2], v0[3]), act1(v1[0], v1[1]), act1(v1[2], v1[3])); } }
	s_nop 0
	v_mul_f32_e32 v23, v23, v28
	v_mul_f32_e32 v23, v25, v23
	v_min_f32_e32 v25, 0x40e00000, v26
	v_med3_f32 v26, v27, s23, v200
	v_mul_f32_e32 v27, 0xc01d265f, v25
	v_exp_f32_e32 v27, v27
	v_pk_fma_f32 v[28:29], v[162:163], s[38:39], v[2:3] op_sel_hi:[1,0,1]
	v_add_f32_e32 v27, 1.0, v27
	v_rcp_f32_e32 v27, v27
	s_nop 0
	v_mul_f32_e32 v25, v25, v27
	v_mul_f32_e32 v25, v26, v25
	v_mov_b32_e32 v26, v195
	v_cvt_pk_fp8_f32 v26, v24, v22
	v_add_co_u32_e32 v22, vcc, s12, v18
	s_mov_b64 s[12:13], 0x10000
	v_cvt_pk_fp8_f32 v26, v23, v25 op_sel:[0,0,1]
	v_pk_fma_f32 v[24:25], v[166:167], s[38:39], v[6:7] op_sel_hi:[1,0,1]
	v_addc_co_u32_e32 v23, vcc, 0, v19, vcc
	v_min_f32_e32 v24, 0x40e00000, v24
	v_mul_f32_e32 v30, 0xc01d265f, v24
	v_exp_f32_e32 v30, v30
	global_store_dword v[22:23], v26, off
	v_pk_fma_f32 v[22:23], v[168:169], s[38:39], v[8:9] op_sel_hi:[1,0,1]
	v_med3_f32 v25, v25, s23, v200
	v_add_f32_e32 v30, 1.0, v30
	v_rcp_f32_e32 v30, v30
	v_min_f32_e32 v22, 0x40e00000, v22
	v_med3_f32 v23, v23, s23, v200
	v_pk_fma_f32 v[26:27], v[164:165], s[38:39], v[4:5] op_sel_hi:[1,0,1]
	v_mul_f32_e32 v24, v24, v30
	v_mul_f32_e32 v24, v25, v24
	v_mul_f32_e32 v25, 0xc01d265f, v22
	v_exp_f32_e32 v25, v25
	s_nop 0
	v_add_f32_e32 v25, 1.0, v25
	v_rcp_f32_e32 v25, v25
	s_nop 0
	v_mul_f32_e32 v22, v22, v25
	v_mul_f32_e32 v22, v23, v22
	v_min_f32_e32 v23, 0x40e00000, v28
	v_mul_f32_e32 v28, 0xc01d265f, v23
	v_exp_f32_e32 v28, v28
	v_med3_f32 v25, v29, s23, v200
	v_add_f32_e32 v28, 1.0, v28
	v_rcp_f32_e32 v28, v28
	s_nop 0
	v_mul_f32_e32 v23, v23, v28
	v_mul_f32_e32 v23, v25, v23
	v_min_f32_e32 v25, 0x40e00000, v26
	v_med3_f32 v26, v27, s23, v200
	v_mul_f32_e32 v27, 0xc01d265f, v25
	v_exp_f32_e32 v27, v27
	v_pk_fma_f32 v[28:29], v[154:155], s[38:39], v[10:11] op_sel_hi:[1,0,1]
	v_add_f32_e32 v27, 1.0, v27
	v_rcp_f32_e32 v27, v27
	s_nop 0
	v_mul_f32_e32 v25, v25, v27
	v_mul_f32_e32 v25, v26, v25
	v_mov_b32_e32 v26, v195
	v_cvt_pk_fp8_f32 v26, v24, v22
	v_cvt_pk_fp8_f32 v26, v23, v25 op_sel:[0,0,1]
	v_pk_fma_f32 v[24:25], v[158:159], s[38:39], v[14:15] op_sel_hi:[1,0,1]
	v_pk_fma_f32 v[22:23], v[160:161], s[38:39], v[16:17] op_sel_hi:[1,0,1]
	v_min_f32_e32 v24, 0x40e00000, v24
	v_mul_f32_e32 v30, 0xc01d265f, v24
	v_exp_f32_e32 v30, v30
	v_med3_f32 v25, v25, s23, v200
	v_min_f32_e32 v22, 0x40e00000, v22
	v_med3_f32 v23, v23, s23, v200
	v_add_f32_e32 v30, 1.0, v30
	v_rcp_f32_e32 v30, v30
	global_store_dword v[20:21], v26, off offset:64
	v_pk_fma_f32 v[26:27], v[156:157], s[38:39], v[12:13] op_sel_hi:[1,0,1]
	v_lshl_add_u64 v[20:21], v[18:19], 0, s[12:13]
	v_mul_f32_e32 v24, v24, v30
	v_mul_f32_e32 v24, v25, v24
	v_mul_f32_e32 v25, 0xc01d265f, v22
	v_exp_f32_e32 v25, v25
	s_mov_b32 s12, 0x10000
	v_add_f32_e32 v25, 1.0, v25
	v_rcp_f32_e32 v25, v25
	s_nop 0
	v_mul_f32_e32 v22, v22, v25
	v_mul_f32_e32 v22, v23, v22
	v_min_f32_e32 v23, 0x40e00000, v28
	v_mul_f32_e32 v28, 0xc01d265f, v23
	v_exp_f32_e32 v28, v28
	v_med3_f32 v25, v29, s23, v200
	v_add_f32_e32 v28, 1.0, v28
	v_rcp_f32_e32 v28, v28
	s_nop 0
	v_mul_f32_e32 v23, v23, v28
	v_mul_f32_e32 v23, v25, v23
	v_min_f32_e32 v25, 0x40e00000, v26
	v_med3_f32 v26, v27, s23, v200
	v_mul_f32_e32 v27, 0xc01d265f, v25
	v_exp_f32_e32 v27, v27
	v_pk_fma_f32 v[28:29], v[146:147], s[38:39], v[2:3] op_sel_hi:[1,0,1]
	v_add_f32_e32 v27, 1.0, v27
	v_rcp_f32_e32 v27, v27
	s_nop 0
	v_mul_f32_e32 v25, v25, v27
	v_mul_f32_e32 v25, v26, v25
	v_mov_b32_e32 v26, v195
	v_cvt_pk_fp8_f32 v26, v24, v22
	v_add_co_u32_e32 v22, vcc, s12, v18
	s_mov_b64 s[12:13], 0x18000
	v_cvt_pk_fp8_f32 v26, v23, v25 op_sel:[0,0,1]
	v_pk_fma_f32 v[24:25], v[150:151], s[38:39], v[6:7] op_sel_hi:[1,0,1]
	v_addc_co_u32_e32 v23, vcc, 0, v19, vcc
	v_min_f32_e32 v24, 0x40e00000, v24
	v_mul_f32_e32 v30, 0xc01d265f, v24
	v_exp_f32_e32 v30, v30
	global_store_dword v[22:23], v26, off
	v_pk_fma_f32 v[22:23], v[152:153], s[38:39], v[8:9] op_sel_hi:[1,0,1]
	v_med3_f32 v25, v25, s23, v200
	v_add_f32_e32 v30, 1.0, v30
	v_rcp_f32_e32 v30, v30
	v_min_f32_e32 v22, 0x40e00000, v22
	v_med3_f32 v23, v23, s23, v200
	v_pk_fma_f32 v[26:27], v[148:149], s[38:39], v[4:5] op_sel_hi:[1,0,1]
	v_mul_f32_e32 v24, v24, v30
	v_mul_f32_e32 v24, v25, v24
	v_mul_f32_e32 v25, 0xc01d265f, v22
	v_exp_f32_e32 v25, v25
	s_nop 0
	v_add_f32_e32 v25, 1.0, v25
	v_rcp_f32_e32 v25, v25
	s_nop 0
	v_mul_f32_e32 v22, v22, v25
	v_mul_f32_e32 v22, v23, v22
	v_min_f32_e32 v23, 0x40e00000, v28
	v_mul_f32_e32 v28, 0xc01d265f, v23
	v_exp_f32_e32 v28, v28
	v_med3_f32 v25, v29, s23, v200
	v_add_f32_e32 v28, 1.0, v28
	v_rcp_f32_e32 v28, v28
	s_nop 0
	v_mul_f32_e32 v23, v23, v28
	v_mul_f32_e32 v23, v25, v23
	v_min_f32_e32 v25, 0x40e00000, v26
	v_med3_f32 v26, v27, s23, v200
	v_mul_f32_e32 v27, 0xc01d265f, v25
	v_exp_f32_e32 v27, v27
	v_pk_fma_f32 v[28:29], v[138:139], s[38:39], v[10:11] op_sel_hi:[1,0,1]
	v_add_f32_e32 v27, 1.0, v27
	v_rcp_f32_e32 v27, v27
	s_nop 0
	v_mul_f32_e32 v25, v25, v27
	v_mul_f32_e32 v25, v26, v25
	v_mov_b32_e32 v26, v195
	v_cvt_pk_fp8_f32 v26, v24, v22
	v_cvt_pk_fp8_f32 v26, v23, v25 op_sel:[0,0,1]
	v_pk_fma_f32 v[24:25], v[142:143], s[38:39], v[14:15] op_sel_hi:[1,0,1]
	v_pk_fma_f32 v[22:23], v[144:145], s[38:39], v[16:17] op_sel_hi:[1,0,1]
	v_min_f32_e32 v24, 0x40e00000, v24
	v_mul_f32_e32 v30, 0xc01d265f, v24
	v_exp_f32_e32 v30, v30
	v_med3_f32 v25, v25, s23, v200
	v_min_f32_e32 v22, 0x40e00000, v22
	v_med3_f32 v23, v23, s23, v200
	v_add_f32_e32 v30, 1.0, v30
	v_rcp_f32_e32 v30, v30
	global_store_dword v[20:21], v26, off offset:64
	v_pk_fma_f32 v[26:27], v[140:141], s[38:39], v[12:13] op_sel_hi:[1,0,1]
	v_lshl_add_u64 v[20:21], v[18:19], 0, s[12:13]
	v_mul_f32_e32 v24, v24, v30
; __device__ __forceinline__ unsigned pk4_fp8(float a, float b, float c, float d) { int p = 0; p = __builtin_amdgcn_cvt_pk_fp8_f32(a, b, p, false); p = __builtin_amdgcn_cvt_pk_fp8_f32(c, d, p, true); return (unsigned)p; }
;     __device__ __forceinline__ float act1(float g, float up1) const { g = fminf(g, 7.f); up1 = fminf(fmaxf(up1, -6.f), 8.f); return g * __builtin_amdgcn_rcpf(1.f + __builtin_amdgcn_exp2f(g * (-1.702f * 1.44269504f))) * up1; }
;     __device__ __forceinline__ void operator()(const f32x4 (&acc)[2][2][4][2], const Unit& u, int wr, int wc, int fr, int fq) const {
;         const int row0 = poff[u.e] + u.pm * BM + wr * 64 + fr, col0 = u.pn * BM + wc * 32 + 8 * fq;
;         const float* bp = bias + (size_t)u.e * (2 * DFF) + col0;
;         f32x4 bv[2][2];
; #pragma unroll
;         for (int bj = 0; bj < 2; ++bj)
; #pragma unroll
;             for (int n = 0; n < 2; ++n) { bv[bj][n] = *(const f32x4*)(bp + bj * HALF + 4 * n); bv[bj][n].y += 1.f; bv[bj][n].w += 1.f; }
; #pragma unroll
;         for (int ai = 0; ai < 2; ++ai)
; #pragma unroll
;             for (int m = 0; m < 4; ++m) { unsigned char* rowp = ACT + (size_t)(row0 + ai * HALF + m * 16) * DFF + (col0 >> 1);
; #pragma unroll
;                 for (int bj = 0; bj < 2; ++bj) { const f32x4 v0 = acc[ai][bj][m][0] * WINV + bv[bj][0], v1 = acc[ai][bj][m][1] * WINV + bv[bj][1];
;                     *(unsigned*)(rowp + bj * (HALF / 2)) = pk4_fp8(act1(v0[0], v0[1]), act1(v0[2], v0[3]), act1(v1[0], v1[1]), act1(v1[2], v1[3])); } }
	v_mul_f32_e32 v24, v25, v24
	v_mul_f32_e32 v25, 0xc01d265f, v22
	v_exp_f32_e32 v25, v25
	s_mov_b32 s12, 0x18000
	v_add_f32_e32 v25, 1.0, v25
	v_rcp_f32_e32 v25, v25
	s_nop 0
	v_mul_f32_e32 v22, v22, v25
	v_mul_f32_e32 v22, v23, v22
	v_min_f32_e32 v23, 0x40e00000, v28
	v_mul_f32_e32 v28, 0xc01d265f, v23
	v_exp_f32_e32 v28, v28
	v_med3_f32 v25, v29, s23, v200
	v_add_f32_e32 v28, 1.0, v28
	v_rcp_f32_e32 v28, v28
	s_nop 0
	v_mul_f32_e32 v23, v23, v28
	v_mul_f32_e32 v23, v25, v23
	v_min_f32_e32 v25, 0x40e00000, v26
	v_med3_f32 v26, v27, s23, v200
	v_mul_f32_e32 v27, 0xc01d265f, v25
	v_exp_f32_e32 v27, v27
	v_pk_fma_f32 v[28:29], v[130:131], s[38:39], v[2:3] op_sel_hi:[1,0,1]
	v_add_f32_e32 v27, 1.0, v27
	v_rcp_f32_e32 v27, v27
	s_nop 0
	v_mul_f32_e32 v25, v25, v27
	v_mul_f32_e32 v25, v26, v25
	v_mov_b32_e32 v26, v195
	v_cvt_pk_fp8_f32 v26, v24, v22
	v_add_co_u32_e32 v22, vcc, s12, v18
	s_mov_b64 s[12:13], 0x40000
	v_cvt_pk_fp8_f32 v26, v23, v25 op_sel:[0,0,1]
	v_pk_fma_f32 v[24:25], v[134:135], s[38:39], v[6:7] op_sel_hi:[1,0,1]
	v_addc_co_u32_e32 v23, vcc, 0, v19, vcc
	v_min_f32_e32 v24, 0x40e00000, v24
	v_mul_f32_e32 v30, 0xc01d265f, v24
	v_exp_f32_e32 v30, v30
	global_store_dword v[22:23], v26, off
	v_pk_fma_f32 v[22:23], v[136:137], s[38:39], v[8:9] op_sel_hi:[1,0,1]
	v_med3_f32 v25, v25, s23, v200
	v_add_f32_e32 v30, 1.0, v30
	v_rcp_f32_e32 v30, v30
	v_min_f32_e32 v22, 0x40e00000, v22
	v_med3_f32 v23, v23, s23, v200
	v_pk_fma_f32 v[26:27], v[132:133], s[38:39], v[4:5] op_sel_hi:[1,0,1]
	v_mul_f32_e32 v24, v24, v30
	v_mul_f32_e32 v24, v25, v24
	v_mul_f32_e32 v25, 0xc01d265f, v22
	v_exp_f32_e32 v25, v25
	s_nop 0
	v_add_f32_e32 v25, 1.0, v25
	v_rcp_f32_e32 v25, v25
	s_nop 0
	v_mul_f32_e32 v22, v22, v25
	v_mul_f32_e32 v22, v23, v22
	v_min_f32_e32 v23, 0x40e00000, v28
	v_mul_f32_e32 v28, 0xc01d265f, v23
	v_exp_f32_e32 v28, v28
	v_med3_f32 v25, v29, s23, v200
	v_add_f32_e32 v28, 1.0, v28
	v_rcp_f32_e32 v28, v28
	s_nop 0
	v_mul_f32_e32 v23, v23, v28
	v_mul_f32_e32 v23, v25, v23
	v_min_f32_e32 v25, 0x40e00000, v26
	v_med3_f32 v26, v27, s23, v200
	v_mul_f32_e32 v27, 0xc01d265f, v25
	v_exp_f32_e32 v27, v27
	v_pk_fma_f32 v[28:29], v[122:123], s[38:39], v[10:11] op_sel_hi:[1,0,1]
	v_add_f32_e32 v27, 1.0, v27
	v_rcp_f32_e32 v27, v27
	s_nop 0
	v_mul_f32_e32 v25, v25, v27
	v_mul_f32_e32 v25, v26, v25
	v_mov_b32_e32 v26, v195
	v_cvt_pk_fp8_f32 v26, v24, v22
	v_cvt_pk_fp8_f32 v26, v23, v25 op_sel:[0,0,1]
	v_pk_fma_f32 v[24:25], v[126:127], s[38:39], v[14:15] op_sel_hi:[1,0,1]
	v_pk_fma_f32 v[22:23], v[128:129], s[38:39], v[16:17] op_sel_hi:[1,0,1]
	v_min_f32_e32 v24, 0x40e00000, v24
	v_mul_f32_e32 v30, 0xc01d265f, v24
	v_exp_f32_e32 v30, v30
	v_med3_f32 v25, v25, s23, v200
	v_min_f32_e32 v22, 0x40e00000, v22
	v_med3_f32 v23, v23, s23, v200
	v_add_f32_e32 v30, 1.0, v30
	v_rcp_f32_e32 v30, v30
	global_store_dword v[20:21], v26, off offset:64
	v_pk_fma_f32 v[26:27], v[124:125], s[38:39], v[12:13] op_sel_hi:[1,0,1]
	v_lshl_add_u64 v[20:21], v[18:19], 0, s[12:13]
	v_mul_f32_e32 v24, v24, v30
	v_mul_f32_e32 v24, v25, v24
	v_mul_f32_e32 v25, 0xc01d265f, v22
	v_exp_f32_e32 v25, v25
	s_mov_b64 s[12:13], 0x48000
	v_add_f32_e32 v25, 1.0, v25
	v_rcp_f32_e32 v25, v25
	s_nop 0
	v_mul_f32_e32 v22, v22, v25
	v_mul_f32_e32 v22, v23, v22
	v_min_f32_e32 v23, 0x40e00000, v28
	v_mul_f32_e32 v28, 0xc01d265f, v23
	v_exp_f32_e32 v28, v28
	v_med3_f32 v25, v29, s23, v200
	v_add_f32_e32 v28, 1.0, v28
	v_rcp_f32_e32 v28, v28
	s_nop 0
	v_mul_f32_e32 v23, v23, v28
	v_mul_f32_e32 v23, v25, v23
	v_min_f32_e32 v25, 0x40e00000, v26
	v_med3_f32 v26, v27, s23, v200
	v_mul_f32_e32 v27, 0xc01d265f, v25
	v_exp_f32_e32 v27, v27
	v_pk_fma_f32 v[28:29], v[114:115], s[38:39], v[2:3] op_sel_hi:[1,0,1]
	v_add_f32_e32 v27, 1.0, v27
	v_rcp_f32_e32 v27, v27
	s_nop 0
	v_mul_f32_e32 v25, v25, v27
	v_mul_f32_e32 v25, v26, v25
	v_mov_b32_e32 v26, v195
	v_cvt_pk_fp8_f32 v26, v24, v22
	v_add_co_u32_e32 v22, vcc, s8, v18
	v_cvt_pk_fp8_f32 v26, v23, v25 op_sel:[0,0,1]
	v_pk_fma_f32 v[24:25], v[118:119], s[38:39], v[6:7] op_sel_hi:[1,0,1]
	v_addc_co_u32_e32 v23, vcc, 0, v19, vcc
	v_min_f32_e32 v24, 0x40e00000, v24
	v_mul_f32_e32 v30, 0xc01d265f, v24
	v_exp_f32_e32 v30, v30
	global_store_dword v[22:23], v26, off
	v_pk_fma_f32 v[22:23], v[120:121], s[38:39], v[8:9] op_sel_hi:[1,0,1]
	v_med3_f32 v25, v25, s23, v200
	v_add_f32_e32 v30, 1.0, v30
	v_rcp_f32_e32 v30, v30
	v_min_f32_e32 v22, 0x40e00000, v22
	v_med3_f32 v23, v23, s23, v200
	v_pk_fma_f32 v[26:27], v[116:117], s[38:39], v[4:5] op_sel_hi:[1,0,1]
	v_mul_f32_e32 v24, v24, v30
	v_mul_f32_e32 v24, v25, v24
	v_mul_f32_e32 v25, 0xc01d265f, v22
	v_exp_f32_e32 v25, v25
	s_nop 0
	v_add_f32_e32 v25, 1.0, v25
	v_rcp_f32_e32 v25, v25
	s_nop 0
	v_mul_f32_e32 v22, v22, v25
	v_mul_f32_e32 v22, v23, v22
	v_min_f32_e32 v23, 0x40e00000, v28
	v_mul_f32_e32 v28, 0xc01d265f, v23
	v_exp_f32_e32 v28, v28
	v_med3_f32 v25, v29, s23, v200
	v_add_f32_e32 v28, 1.0, v28
	v_rcp_f32_e32 v28, v28
	s_nop 0
	v_mul_f32_e32 v23, v23, v28
	v_mul_f32_e32 v23, v25, v23
	v_min_f32_e32 v25, 0x40e00000, v26
	v_med3_f32 v26, v27, s23, v200
	v_mul_f32_e32 v27, 0xc01d265f, v25
	v_exp_f32_e32 v27, v27
	v_pk_fma_f32 v[28:29], v[106:107], s[38:39], v[10:11] op_sel_hi:[1,0,1]
	v_add_f32_e32 v27, 1.0, v27
	v_rcp_f32_e32 v27, v27
	s_nop 0
	v_mul_f32_e32 v25, v25, v27
	v_mul_f32_e32 v25, v26, v25
	v_mov_b32_e32 v26, v195
	v_cvt_pk_fp8_f32 v26, v24, v22
	v_cvt_pk_fp8_f32 v26, v23, v25 op_sel:[0,0,1]
	v_pk_fma_f32 v[24:25], v[110:111], s[38:39], v[14:15] op_sel_hi:[1,0,1]
	v_pk_fma_f32 v[22:23], v[112:113], s[38:39], v[16:17] op_sel_hi:[1,0,1]
	v_min_f32_e32 v24, 0x40e00000, v24
	v_mul_f32_e32 v30, 0xc01d265f, v24
; __device__ __forceinline__ unsigned pk4_fp8(float a, float b, float c, float d) { int p = 0; p = __builtin_amdgcn_cvt_pk_fp8_f32(a, b, p, false); p = __builtin_amdgcn_cvt_pk_fp8_f32(c, d, p, true); return (unsigned)p; }
;     __device__ __forceinline__ float act1(float g, float up1) const { g = fminf(g, 7.f); up1 = fminf(fmaxf(up1, -6.f), 8.f); return g * __builtin_amdgcn_rcpf(1.f + __builtin_amdgcn_exp2f(g * (-1.702f * 1.44269504f))) * up1; }
;     __device__ __forceinline__ void operator()(const f32x4 (&acc)[2][2][4][2], const Unit& u, int wr, int wc, int fr, int fq) const {
;         const int row0 = poff[u.e] + u.pm * BM + wr * 64 + fr, col0 = u.pn * BM + wc * 32 + 8 * fq;
;         const float* bp = bias + (size_t)u.e * (2 * DFF) + col0;
;         f32x4 bv[2][2];
; #pragma unroll
;         for (int bj = 0; bj < 2; ++bj)
; #pragma unroll
;             for (int n = 0; n < 2; ++n) { bv[bj][n] = *(const f32x4*)(bp + bj * HALF + 4 * n); bv[bj][n].y += 1.f; bv[bj][n].w += 1.f; }
; #pragma unroll
;         for (int ai = 0; ai < 2; ++ai)
; #pragma unroll
;             for (int m = 0; m < 4; ++m) { unsigned char* rowp = ACT + (size_t)(row0 + ai * HALF + m * 16) * DFF + (col0 >> 1);
; #pragma unroll
;                 for (int bj = 0; bj < 2; ++bj) { const f32x4 v0 = acc[ai][bj][m][0] * WINV + bv[bj][0], v1 = acc[ai][bj][m][1] * WINV + bv[bj][1];
;                     *(unsigned*)(rowp + bj * (HALF / 2)) = pk4_fp8(act1(v0[0], v0[1]), act1(v0[2], v0[3]), act1(v1[0], v1[1]), act1(v1[2], v1[3])); } }
	v_exp_f32_e32 v30, v30
	v_med3_f32 v25, v25, s23, v200
	v_min_f32_e32 v22, 0x40e00000, v22
	v_med3_f32 v23, v23, s23, v200
	v_add_f32_e32 v30, 1.0, v30
	v_rcp_f32_e32 v30, v30
	global_store_dword v[20:21], v26, off offset:64
	v_pk_fma_f32 v[26:27], v[108:109], s[38:39], v[12:13] op_sel_hi:[1,0,1]
	v_lshl_add_u64 v[20:21], v[18:19], 0, s[12:13]
	v_mul_f32_e32 v24, v24, v30
	v_mul_f32_e32 v24, v25, v24
	v_mul_f32_e32 v25, 0xc01d265f, v22
	v_exp_f32_e32 v25, v25
	s_mov_b32 s12, 0x48000
	v_add_f32_e32 v25, 1.0, v25
	v_rcp_f32_e32 v25, v25
	s_nop 0
	v_mul_f32_e32 v22, v22, v25
	v_mul_f32_e32 v22, v23, v22
	v_min_f32_e32 v23, 0x40e00000, v28
	v_mul_f32_e32 v28, 0xc01d265f, v23
	v_exp_f32_e32 v28, v28
	v_med3_f32 v25, v29, s23, v200
	v_add_f32_e32 v28, 1.0, v28
	v_rcp_f32_e32 v28, v28
	s_nop 0
	v_mul_f32_e32 v23, v23, v28
	v_mul_f32_e32 v23, v25, v23
	v_min_f32_e32 v25, 0x40e00000, v26
	v_med3_f32 v26, v27, s23, v200
	v_mul_f32_e32 v27, 0xc01d265f, v25
	v_exp_f32_e32 v27, v27
	v_pk_fma_f32 v[28:29], v[98:99], s[38:39], v[2:3] op_sel_hi:[1,0,1]
	v_add_f32_e32 v27, 1.0, v27
	v_rcp_f32_e32 v27, v27
	s_nop 0
	v_mul_f32_e32 v25, v25, v27
	v_mul_f32_e32 v25, v26, v25
	v_mov_b32_e32 v26, v195
	v_cvt_pk_fp8_f32 v26, v24, v22
	v_add_co_u32_e32 v22, vcc, s12, v18
	s_mov_b64 s[12:13], 0x50000
	v_cvt_pk_fp8_f32 v26, v23, v25 op_sel:[0,0,1]
	v_pk_fma_f32 v[24:25], v[102:103], s[38:39], v[6:7] op_sel_hi:[1,0,1]
	v_addc_co_u32_e32 v23, vcc, 0, v19, vcc
	v_min_f32_e32 v24, 0x40e00000, v24
	v_mul_f32_e32 v30, 0xc01d265f, v24
	v_exp_f32_e32 v30, v30
	global_store_dword v[22:23], v26, off
	v_pk_fma_f32 v[22:23], v[104:105], s[38:39], v[8:9] op_sel_hi:[1,0,1]
	v_med3_f32 v25, v25, s23, v200
	v_add_f32_e32 v30, 1.0, v30
	v_rcp_f32_e32 v30, v30
	v_min_f32_e32 v22, 0x40e00000, v22
	v_med3_f32 v23, v23, s23, v200
	v_pk_fma_f32 v[26:27], v[100:101], s[38:39], v[4:5] op_sel_hi:[1,0,1]
	v_mul_f32_e32 v24, v24, v30
	v_mul_f32_e32 v24, v25, v24
	v_mul_f32_e32 v25, 0xc01d265f, v22
	v_exp_f32_e32 v25, v25
	s_nop 0
	v_add_f32_e32 v25, 1.0, v25
	v_rcp_f32_e32 v25, v25
	s_nop 0
	v_mul_f32_e32 v22, v22, v25
	v_mul_f32_e32 v22, v23, v22
	v_min_f32_e32 v23, 0x40e00000, v28
	v_mul_f32_e32 v28, 0xc01d265f, v23
	v_exp_f32_e32 v28, v28
	v_med3_f32 v25, v29, s23, v200
	v_add_f32_e32 v28, 1.0, v28
	v_rcp_f32_e32 v28, v28
	s_nop 0
	v_mul_f32_e32 v23, v23, v28
	v_mul_f32_e32 v23, v25, v23
	v_min_f32_e32 v25, 0x40e00000, v26
	v_med3_f32 v26, v27, s23, v200
	v_mul_f32_e32 v27, 0xc01d265f, v25
	v_exp_f32_e32 v27, v27
	v_pk_fma_f32 v[28:29], v[90:91], s[38:39], v[10:11] op_sel_hi:[1,0,1]
	v_pk_fma_f32 v[10:11], v[74:75], s[38:39], v[10:11] op_sel_hi:[1,0,1]
	v_add_f32_e32 v27, 1.0, v27
	v_rcp_f32_e32 v27, v27
	v_min_f32_e32 v10, 0x40e00000, v10
	v_med3_f32 v11, v11, s23, v200
	v_mul_f32_e32 v25, v25, v27
	v_mul_f32_e32 v25, v26, v25
	v_mov_b32_e32 v26, v195
	v_cvt_pk_fp8_f32 v26, v24, v22
	v_cvt_pk_fp8_f32 v26, v23, v25 op_sel:[0,0,1]
	v_pk_fma_f32 v[24:25], v[94:95], s[38:39], v[14:15] op_sel_hi:[1,0,1]
	v_pk_fma_f32 v[22:23], v[96:97], s[38:39], v[16:17] op_sel_hi:[1,0,1]
	v_min_f32_e32 v24, 0x40e00000, v24
	v_mul_f32_e32 v30, 0xc01d265f, v24
	v_exp_f32_e32 v30, v30
	v_med3_f32 v25, v25, s23, v200
	v_min_f32_e32 v22, 0x40e00000, v22
	v_med3_f32 v23, v23, s23, v200
	v_add_f32_e32 v30, 1.0, v30
	v_rcp_f32_e32 v30, v30
	global_store_dword v[20:21], v26, off offset:64
	v_pk_fma_f32 v[26:27], v[92:93], s[38:39], v[12:13] op_sel_hi:[1,0,1]
	v_lshl_add_u64 v[20:21], v[18:19], 0, s[12:13]
	v_mul_f32_e32 v24, v24, v30
	v_mul_f32_e32 v24, v25, v24
	v_mul_f32_e32 v25, 0xc01d265f, v22
	v_exp_f32_e32 v25, v25
	s_mov_b32 s12, 0x50000
	v_pk_fma_f32 v[14:15], v[78:79], s[38:39], v[14:15] op_sel_hi:[1,0,1]
	v_pk_fma_f32 v[16:17], v[80:81], s[38:39], v[16:17] op_sel_hi:[1,0,1]
	v_add_f32_e32 v25, 1.0, v25
	v_rcp_f32_e32 v25, v25
	v_min_f32_e32 v14, 0x40e00000, v14
	v_med3_f32 v15, v15, s23, v200
	v_pk_fma_f32 v[12:13], v[76:77], s[38:39], v[12:13] op_sel_hi:[1,0,1]
	v_mul_f32_e32 v22, v22, v25
	v_mul_f32_e32 v22, v23, v22
	v_min_f32_e32 v23, 0x40e00000, v28
	v_mul_f32_e32 v28, 0xc01d265f, v23
	v_exp_f32_e32 v28, v28
	v_med3_f32 v25, v29, s23, v200
	v_add_f32_e32 v28, 1.0, v28
	v_rcp_f32_e32 v28, v28
	s_nop 0
	v_mul_f32_e32 v23, v23, v28
	v_mul_f32_e32 v23, v25, v23
	v_min_f32_e32 v25, 0x40e00000, v26
	v_med3_f32 v26, v27, s23, v200
	v_mul_f32_e32 v27, 0xc01d265f, v25
	v_exp_f32_e32 v27, v27
; __device__ __forceinline__ int fresh_lane() { int l = (int)__builtin_amdgcn_mbcnt_hi(~0u, __builtin_amdgcn_mbcnt_lo(~0u, 0u)); asm volatile("" : "+v"(l)); return l; }
; __device__ __forceinline__ unsigned pk4_fp8(float a, float b, float c, float d) { int p = 0; p = __builtin_amdgcn_cvt_pk_fp8_f32(a, b, p, false); p = __builtin_amdgcn_cvt_pk_fp8_f32(c, d, p, true); return (unsigned)p; }
; #define PG8_BAR __builtin_amdgcn_s_barrier()
;     __device__ __forceinline__ float act1(float g, float up1) const { g = fminf(g, 7.f); up1 = fminf(fmaxf(up1, -6.f), 8.f); return g * __builtin_amdgcn_rcpf(1.f + __builtin_amdgcn_exp2f(g * (-1.702f * 1.44269504f))) * up1; }
;     __device__ __forceinline__ void operator()(const f32x4 (&acc)[2][2][4][2], const Unit& u, int wr, int wc, int fr, int fq) const {
;         const int row0 = poff[u.e] + u.pm * BM + wr * 64 + fr, col0 = u.pn * BM + wc * 32 + 8 * fq;
;         const float* bp = bias + (size_t)u.e * (2 * DFF) + col0;
;         f32x4 bv[2][2];
; #pragma unroll
;         for (int bj = 0; bj < 2; ++bj)
; #pragma unroll
;             for (int n = 0; n < 2; ++n) { bv[bj][n] = *(const f32x4*)(bp + bj * HALF + 4 * n); bv[bj][n].y += 1.f; bv[bj][n].w += 1.f; }
; #pragma unroll
;         for (int ai = 0; ai < 2; ++ai)
; #pragma unroll
;             for (int m = 0; m < 4; ++m) { unsigned char* rowp = ACT + (size_t)(row0 + ai * HALF + m * 16) * DFF + (col0 >> 1);
; #pragma unroll
;                 for (int bj = 0; bj < 2; ++bj) { const f32x4 v0 = acc[ai][bj][m][0] * WINV + bv[bj][0], v1 = acc[ai][bj][m][1] * WINV + bv[bj][1];
;                     *(unsigned*)(rowp + bj * (HALF / 2)) = pk4_fp8(act1(v0[0], v0[1]), act1(v0[2], v0[3]), act1(v1[0], v1[1]), act1(v1[2], v1[3])); } }
; template <class Epi, class Sched>
; __device__ __forceinline__ void gemm_phase(LAS unsigned char* lds, const Sched& S, const Epi& E) {
;     ...
;         if (wr == 0) PG8_BAR;
;         { const int l2 = fresh_lane(); E(acc, cur, wr, wc, l2 & 15, l2 >> 4); }
;         if (!has_next) break;
; #pragma unroll
;         for (int a = 0; a < 2; ++a)
; #pragma unroll
;             for (int b = 0; b < 2; ++b)
; #pragma unroll
;                 for (int m = 0; m < 4; ++m)
; #pragma unroll
;                     for (int n = 0; n < 2; ++n) acc[a][b][m][n] = (f32x4){0.f, 0.f, 0.f, 0.f};
;         cur = nxt; cA = nA; cB = nB; ++ui;
;         if (wr == 1) PG8_BAR;
;     }
	v_pk_fma_f32 v[28:29], v[82:83], s[38:39], v[2:3] op_sel_hi:[1,0,1]
	v_pk_fma_f32 v[2:3], v[66:67], s[38:39], v[2:3] op_sel_hi:[1,0,1]
	v_add_f32_e32 v27, 1.0, v27
	v_rcp_f32_e32 v27, v27
	v_min_f32_e32 v2, 0x40e00000, v2
	v_med3_f32 v3, v3, s23, v200
	v_mul_f32_e32 v25, v25, v27
	v_mul_f32_e32 v25, v26, v25
	v_mov_b32_e32 v26, v195
	v_cvt_pk_fp8_f32 v26, v24, v22
	v_add_co_u32_e32 v22, vcc, s12, v18
	s_mov_b64 s[12:13], 0x58000
	v_cvt_pk_fp8_f32 v26, v23, v25 op_sel:[0,0,1]
	v_pk_fma_f32 v[24:25], v[86:87], s[38:39], v[6:7] op_sel_hi:[1,0,1]
	v_addc_co_u32_e32 v23, vcc, 0, v19, vcc
	v_min_f32_e32 v24, 0x40e00000, v24
	v_mul_f32_e32 v30, 0xc01d265f, v24
	v_exp_f32_e32 v30, v30
	global_store_dword v[22:23], v26, off
	v_pk_fma_f32 v[22:23], v[88:89], s[38:39], v[8:9] op_sel_hi:[1,0,1]
	v_med3_f32 v25, v25, s23, v200
	v_add_f32_e32 v30, 1.0, v30
	v_rcp_f32_e32 v30, v30
	v_min_f32_e32 v22, 0x40e00000, v22
	v_med3_f32 v23, v23, s23, v200
	v_pk_fma_f32 v[26:27], v[84:85], s[38:39], v[4:5] op_sel_hi:[1,0,1]
	v_mul_f32_e32 v24, v24, v30
	v_mul_f32_e32 v24, v25, v24
	v_mul_f32_e32 v25, 0xc01d265f, v22
	v_exp_f32_e32 v25, v25
	v_pk_fma_f32 v[6:7], v[70:71], s[38:39], v[6:7] op_sel_hi:[1,0,1]
	v_pk_fma_f32 v[8:9], v[72:73], s[38:39], v[8:9] op_sel_hi:[1,0,1]
	v_min_f32_e32 v6, 0x40e00000, v6
	v_add_f32_e32 v25, 1.0, v25
	v_rcp_f32_e32 v25, v25
	v_med3_f32 v7, v7, s23, v200
	v_pk_fma_f32 v[4:5], v[68:69], s[38:39], v[4:5] op_sel_hi:[1,0,1]
	v_mul_f32_e32 v22, v22, v25
	v_mul_f32_e32 v22, v23, v22
	v_min_f32_e32 v23, 0x40e00000, v28
	v_mul_f32_e32 v28, 0xc01d265f, v23
	v_exp_f32_e32 v28, v28
	v_med3_f32 v25, v29, s23, v200
	v_add_f32_e32 v28, 1.0, v28
	v_rcp_f32_e32 v28, v28
	s_nop 0
	v_mul_f32_e32 v23, v23, v28
	v_mul_f32_e32 v23, v25, v23
	v_min_f32_e32 v25, 0x40e00000, v26
	v_med3_f32 v26, v27, s23, v200
	v_mul_f32_e32 v27, 0xc01d265f, v25
	v_exp_f32_e32 v27, v27
	s_nop 0
	v_add_f32_e32 v27, 1.0, v27
	v_rcp_f32_e32 v27, v27
	s_nop 0
	v_mul_f32_e32 v25, v25, v27
	v_mul_f32_e32 v25, v26, v25
	v_mov_b32_e32 v26, v195
	v_cvt_pk_fp8_f32 v26, v24, v22
	v_mul_f32_e32 v22, 0xc01d265f, v14
	v_exp_f32_e32 v22, v22
	v_cvt_pk_fp8_f32 v26, v23, v25 op_sel:[0,0,1]
	v_add_f32_e32 v22, 1.0, v22
	v_rcp_f32_e32 v22, v22
	global_store_dword v[20:21], v26, off offset:64
	v_lshl_add_u64 v[20:21], v[18:19], 0, s[12:13]
	s_mov_b32 s12, 0x58000
	v_mul_f32_e32 v14, v14, v22
	v_mul_f32_e32 v14, v15, v14
	v_min_f32_e32 v15, 0x40e00000, v16
	v_med3_f32 v16, v17, s23, v200
	v_mul_f32_e32 v17, 0xc01d265f, v15
	v_exp_f32_e32 v17, v17
	s_nop 0
	v_add_f32_e32 v17, 1.0, v17
	v_rcp_f32_e32 v17, v17
	s_nop 0
	v_mul_f32_e32 v15, v15, v17
	v_mul_f32_e32 v15, v16, v15
	v_mul_f32_e32 v16, 0xc01d265f, v10
	v_exp_f32_e32 v16, v16
	s_nop 0
	v_add_f32_e32 v16, 1.0, v16
	v_rcp_f32_e32 v16, v16
	s_nop 0
	v_mul_f32_e32 v10, v10, v16
	v_mul_f32_e32 v10, v11, v10
	v_min_f32_e32 v11, 0x40e00000, v12
	v_med3_f32 v12, v13, s23, v200
	v_mul_f32_e32 v13, 0xc01d265f, v11
	v_exp_f32_e32 v13, v13
	s_nop 0
	v_add_f32_e32 v13, 1.0, v13
	v_rcp_f32_e32 v13, v13
	s_nop 0
	v_mul_f32_e32 v11, v11, v13
	v_mul_f32_e32 v11, v12, v11
	v_mov_b32_e32 v12, v195
	v_cvt_pk_fp8_f32 v12, v14, v15
	v_cvt_pk_fp8_f32 v12, v10, v11 op_sel:[0,0,1]
	v_add_co_u32_e32 v10, vcc, s12, v18
	s_nop 1
	v_addc_co_u32_e32 v11, vcc, 0, v19, vcc
	global_store_dword v[10:11], v12, off
	v_mul_f32_e32 v10, 0xc01d265f, v6
	v_exp_f32_e32 v10, v10
	s_and_b64 vcc, exec, s[2:3]
	v_add_f32_e32 v10, 1.0, v10
	v_rcp_f32_e32 v10, v10
	s_nop 0
	v_mul_f32_e32 v6, v6, v10
	v_mul_f32_e32 v6, v7, v6
	v_min_f32_e32 v7, 0x40e00000, v8
	v_med3_f32 v8, v9, s23, v200
	v_mul_f32_e32 v9, 0xc01d265f, v7
	v_exp_f32_e32 v9, v9
	s_nop 0
	v_add_f32_e32 v9, 1.0, v9
	v_rcp_f32_e32 v9, v9
	s_nop 0
	v_mul_f32_e32 v7, v7, v9
	v_mul_f32_e32 v7, v8, v7
	v_mul_f32_e32 v8, 0xc01d265f, v2
	v_exp_f32_e32 v8, v8
	s_nop 0
	v_add_f32_e32 v8, 1.0, v8
	v_rcp_f32_e32 v8, v8
	s_nop 0
	v_mul_f32_e32 v2, v2, v8
	v_mul_f32_e32 v2, v3, v2
	v_min_f32_e32 v3, 0x40e00000, v4
	v_med3_f32 v4, v5, s23, v200
	v_mul_f32_e32 v5, 0xc01d265f, v3
	v_exp_f32_e32 v5, v5
	s_nop 0
	v_add_f32_e32 v5, 1.0, v5
	v_rcp_f32_e32 v5, v5
	s_nop 0
	v_mul_f32_e32 v3, v3, v5
	v_mul_f32_e32 v3, v4, v3
	v_mov_b32_e32 v4, v195
	v_cvt_pk_fp8_f32 v4, v6, v7
	v_cvt_pk_fp8_f32 v4, v2, v3 op_sel:[0,0,1]
	global_store_dword v[20:21], v4, off offset:64
	s_cbranch_vccnz .LBB0_1001
	s_andn2_b64 vcc, exec, s[0:1]
	s_cbranch_vccnz .LBB0_1000
	s_barrier
	s_branch .LBB0_1000

; __device__ __forceinline__ unsigned pk4_fp8(float a, float b, float c, float d) { int p = 0; p = __builtin_amdgcn_cvt_pk_fp8_f32(a, b, p, false); p = __builtin_amdgcn_cvt_pk_fp8_f32(c, d, p, true); return (unsigned)p; }
;     __device__ __forceinline__ void operator()(const f32x4 (&acc)[2][2][4][2], const Unit& u, int wr, int wc, int fr, int fq) const {
;         const int row0 = poff[u.e] + u.pm * BM + wr * 64 + fr, col0 = u.pn * BM + wc * 32 + 8 * fq;
;         const float* bp = bias + (size_t)u.e * D + col0;
; #pragma unroll
;         for (int bj = 0; bj < 2; ++bj) { const f32x4 b0 = *(const f32x4*)(bp + bj * HALF), b1 = *(const f32x4*)(bp + bj * HALF + 4);
; #pragma unroll
;             for (int ai = 0; ai < 2; ++ai)
; #pragma unroll
;                 for (int m = 0; m < 4; ++m) { unsigned char* rowp = YS + (size_t)(row0 + ai * HALF + m * 16) * D + col0 + bj * HALF;
;                     const f32x4 v0 = (acc[ai][bj][m][0] * WINV + b0) * YSCALE, v1 = (acc[ai][bj][m][1] * WINV + b1) * YSCALE;
;                     u32x2 w; w.x = pk4_fp8(v0[0], v0[1], v0[2], v0[3]); w.y = pk4_fp8(v1[0], v1[1], v1[2], v1[3]);
;                     *(u32x2*)rowp = w; } }
.LBB0_1467:
	s_lshl_b32 s27, s40, 2
	s_add_i32 s27, s27, 0
	s_add_i32 s27, s27, 0x20300
	v_mov_b32_e32 v122, v1
	v_mov_b32_e32 v123, s27
	s_ashr_i32 s41, s40, 31
	ds_read_b32 v123, v123
	s_lshl_b32 s29, s84, 8
	v_ashrrev_i32_e32 v124, 1, v122
	s_lshl_b32 s27, s42, 8
	v_and_b32_e32 v124, -8, v124
	s_or_b32 s29, s29, s8
	s_lshl_b64 s[40:41], s[40:41], 13
	v_add_u32_e32 v142, s29, v124
	s_add_u32 s40, s68, s40
	s_addc_u32 s41, s69, s41
	v_ashrrev_i32_e32 v143, 31, v142
	s_add_i32 s27, s27, s78
	v_lshl_add_u64 v[144:145], v[142:143], 2, s[40:41]
	v_and_or_b32 v122, v122, 15, s27
	s_waitcnt lgkmcnt(0)
	v_add_u32_e32 v156, v122, v123
	global_load_dwordx4 v[122:125], v[144:145], off offset:16
	global_load_dwordx4 v[134:137], v[144:145], off
	global_load_dwordx4 v[160:163], v[144:145], off offset:528
	global_load_dwordx4 v[164:167], v[144:145], off offset:512
	v_ashrrev_i32_e32 v157, 31, v156
	v_lshlrev_b64 v[156:157], 11, v[156:157]
	v_lshl_add_u64 v[156:157], s[6:7], 0, v[156:157]
	v_lshl_add_u64 v[142:143], v[156:157], 0, v[142:143]
	v_mov_b32_e32 v157, v139
	s_mov_b32 s27, 0x8000
	v_mov_b32_e32 v156, v139
	s_mov_b64 s[40:41], 0x8000
	s_waitcnt vmcnt(3)
	v_pk_fma_f32 v[126:127], v[126:127], s[18:19], v[122:123] op_sel_hi:[1,0,1]
	s_nop 0
	v_pk_mul_f32 v[126:127], v[126:127], s[20:21] op_sel_hi:[1,0]
	v_pk_fma_f32 v[128:129], v[128:129], s[18:19], v[124:125] op_sel_hi:[1,0,1]
	v_cvt_pk_fp8_f32 v157, v126, v127
	v_pk_mul_f32 v[128:129], v[128:129], s[20:21] op_sel_hi:[1,0]
	v_pk_fma_f32 v[114:115], v[114:115], s[18:19], v[122:123] op_sel_hi:[1,0,1]
	v_pk_fma_f32 v[116:117], v[116:117], s[18:19], v[124:125] op_sel_hi:[1,0,1]
	v_cvt_pk_fp8_f32 v157, v128, v129 op_sel:[0,0,1]
	v_pk_mul_f32 v[114:115], v[114:115], s[20:21] op_sel_hi:[1,0]
	v_mov_b32_e32 v129, v139
	v_cvt_pk_fp8_f32 v129, v114, v115
	v_pk_mul_f32 v[116:117], v[116:117], s[20:21] op_sel_hi:[1,0]
	v_pk_fma_f32 v[106:107], v[106:107], s[18:19], v[122:123] op_sel_hi:[1,0,1]
	v_pk_fma_f32 v[108:109], v[108:109], s[18:19], v[124:125] op_sel_hi:[1,0,1]
	v_cvt_pk_fp8_f32 v129, v116, v117 op_sel:[0,0,1]
	v_pk_mul_f32 v[106:107], v[106:107], s[20:21] op_sel_hi:[1,0]
	v_mov_b32_e32 v117, v139
	v_cvt_pk_fp8_f32 v117, v106, v107
	v_pk_mul_f32 v[108:109], v[108:109], s[20:21] op_sel_hi:[1,0]
	s_waitcnt vmcnt(2)
	v_pk_fma_f32 v[102:103], v[102:103], s[18:19], v[134:135] op_sel_hi:[1,0,1]
	v_pk_fma_f32 v[98:99], v[98:99], s[18:19], v[122:123] op_sel_hi:[1,0,1]
	v_cvt_pk_fp8_f32 v117, v108, v109 op_sel:[0,0,1]
	v_pk_mul_f32 v[102:103], v[102:103], s[20:21] op_sel_hi:[1,0]
	v_pk_mul_f32 v[108:109], v[98:99], s[20:21] op_sel_hi:[1,0]
	v_mov_b32_e32 v98, v139
	v_mov_b32_e32 v99, v139
	v_cvt_pk_fp8_f32 v98, v102, v103
	v_cvt_pk_fp8_f32 v99, v108, v109
	v_add_co_u32_e32 v114, vcc, s27, v142
	v_pk_fma_f32 v[104:105], v[104:105], s[18:19], v[136:137] op_sel_hi:[1,0,1]
	v_pk_fma_f32 v[100:101], v[100:101], s[18:19], v[124:125] op_sel_hi:[1,0,1]
	v_addc_co_u32_e32 v115, vcc, 0, v143, vcc
	s_mov_b32 s27, 0x10000
	v_pk_mul_f32 v[104:105], v[104:105], s[20:21] op_sel_hi:[1,0]
	v_pk_mul_f32 v[100:101], v[100:101], s[20:21] op_sel_hi:[1,0]
	v_add_co_u32_e32 v106, vcc, s27, v142
	v_cvt_pk_fp8_f32 v98, v104, v105 op_sel:[0,0,1]
	v_cvt_pk_fp8_f32 v99, v100, v101 op_sel:[0,0,1]
	v_addc_co_u32_e32 v107, vcc, 0, v143, vcc
	s_mov_b32 s27, 0x18000
	v_add_co_u32_e32 v100, vcc, s27, v142
	v_pk_fma_f32 v[90:91], v[90:91], s[18:19], v[122:123] op_sel_hi:[1,0,1]
	s_nop 0
	v_addc_co_u32_e32 v101, vcc, 0, v143, vcc
	global_store_dwordx2 v[100:101], v[98:99], off
	v_pk_mul_f32 v[90:91], v[90:91], s[20:21] op_sel_hi:[1,0]
	v_mov_b32_e32 v101, v139
	v_cvt_pk_fp8_f32 v101, v90, v91
	v_pk_fma_f32 v[92:93], v[92:93], s[18:19], v[124:125] op_sel_hi:[1,0,1]
	v_pk_fma_f32 v[82:83], v[82:83], s[18:19], v[122:123] op_sel_hi:[1,0,1]
	v_pk_mul_f32 v[92:93], v[92:93], s[20:21] op_sel_hi:[1,0]
	v_pk_mul_f32 v[82:83], v[82:83], s[20:21] op_sel_hi:[1,0]
	v_cvt_pk_fp8_f32 v101, v92, v93 op_sel:[0,0,1]
	v_mov_b32_e32 v93, v139
	v_cvt_pk_fp8_f32 v93, v82, v83
	v_pk_fma_f32 v[84:85], v[84:85], s[18:19], v[124:125] op_sel_hi:[1,0,1]
	v_pk_fma_f32 v[74:75], v[74:75], s[18:19], v[122:123] op_sel_hi:[1,0,1]
	v_pk_mul_f32 v[84:85], v[84:85], s[20:21] op_sel_hi:[1,0]
	v_pk_mul_f32 v[74:75], v[74:75], s[20:21] op_sel_hi:[1,0]
	v_cvt_pk_fp8_f32 v93, v84, v85 op_sel:[0,0,1]
	v_mov_b32_e32 v85, v139
	v_cvt_pk_fp8_f32 v85, v74, v75
	v_pk_fma_f32 v[76:77], v[76:77], s[18:19], v[124:125] op_sel_hi:[1,0,1]
	v_pk_fma_f32 v[130:131], v[130:131], s[18:19], v[134:135] op_sel_hi:[1,0,1]
	v_pk_fma_f32 v[118:119], v[118:119], s[18:19], v[134:135] op_sel_hi:[1,0,1]
	v_pk_fma_f32 v[110:111], v[110:111], s[18:19], v[134:135] op_sel_hi:[1,0,1]
	v_pk_fma_f32 v[94:95], v[94:95], s[18:19], v[134:135] op_sel_hi:[1,0,1]
	v_pk_fma_f32 v[86:87], v[86:87], s[18:19], v[134:135] op_sel_hi:[1,0,1]
	v_pk_fma_f32 v[78:79], v[78:79], s[18:19], v[134:135] op_sel_hi:[1,0,1]
	v_pk_mul_f32 v[76:77], v[76:77], s[20:21] op_sel_hi:[1,0]
	v_pk_fma_f32 v[70:71], v[70:71], s[18:19], v[134:135] op_sel_hi:[1,0,1]
	v_pk_fma_f32 v[66:67], v[66:67], s[18:19], v[122:123] op_sel_hi:[1,0,1]
	v_pk_mul_f32 v[130:131], v[130:131], s[20:21] op_sel_hi:[1,0]
	v_pk_mul_f32 v[118:119], v[118:119], s[20:21] op_sel_hi:[1,0]
	v_mov_b32_e32 v128, v139
	v_pk_mul_f32 v[110:111], v[110:111], s[20:21] op_sel_hi:[1,0]
	v_mov_b32_e32 v116, v139
	v_pk_mul_f32 v[94:95], v[94:95], s[20:21] op_sel_hi:[1,0]
	v_mov_b32_e32 v100, v139
	s_mov_b32 s27, 0x40000
	v_pk_mul_f32 v[86:87], v[86:87], s[20:21] op_sel_hi:[1,0]
	v_mov_b32_e32 v92, v139
	v_pk_mul_f32 v[78:79], v[78:79], s[20:21] op_sel_hi:[1,0]
	v_mov_b32_e32 v84, v139
; __device__ __forceinline__ unsigned pk4_fp8(float a, float b, float c, float d) { int p = 0; p = __builtin_amdgcn_cvt_pk_fp8_f32(a, b, p, false); p = __builtin_amdgcn_cvt_pk_fp8_f32(c, d, p, true); return (unsigned)p; }
;     __device__ __forceinline__ void operator()(const f32x4 (&acc)[2][2][4][2], const Unit& u, int wr, int wc, int fr, int fq) const {
;         const int row0 = poff[u.e] + u.pm * BM + wr * 64 + fr, col0 = u.pn * BM + wc * 32 + 8 * fq;
;         const float* bp = bias + (size_t)u.e * D + col0;
; #pragma unroll
;         for (int bj = 0; bj < 2; ++bj) { const f32x4 b0 = *(const f32x4*)(bp + bj * HALF), b1 = *(const f32x4*)(bp + bj * HALF + 4);
; #pragma unroll
;             for (int ai = 0; ai < 2; ++ai)
; #pragma unroll
;                 for (int m = 0; m < 4; ++m) { unsigned char* rowp = YS + (size_t)(row0 + ai * HALF + m * 16) * D + col0 + bj * HALF;
;                     const f32x4 v0 = (acc[ai][bj][m][0] * WINV + b0) * YSCALE, v1 = (acc[ai][bj][m][1] * WINV + b1) * YSCALE;
;                     u32x2 w; w.x = pk4_fp8(v0[0], v0[1], v0[2], v0[3]); w.y = pk4_fp8(v1[0], v1[1], v1[2], v1[3]);
;                     *(u32x2*)rowp = w; } }
	v_cvt_pk_fp8_f32 v85, v76, v77 op_sel:[0,0,1]
	v_pk_mul_f32 v[70:71], v[70:71], s[20:21] op_sel_hi:[1,0]
	v_pk_mul_f32 v[66:67], v[66:67], s[20:21] op_sel_hi:[1,0]
	v_mov_b32_e32 v76, v139
	v_mov_b32_e32 v77, v139
	v_cvt_pk_fp8_f32 v156, v130, v131
	v_cvt_pk_fp8_f32 v128, v118, v119
	v_cvt_pk_fp8_f32 v116, v110, v111
	v_cvt_pk_fp8_f32 v100, v94, v95
	v_add_co_u32_e32 v90, vcc, s27, v142
	v_cvt_pk_fp8_f32 v92, v86, v87
	v_cvt_pk_fp8_f32 v84, v78, v79
	v_cvt_pk_fp8_f32 v76, v70, v71
	v_cvt_pk_fp8_f32 v77, v66, v67
	v_addc_co_u32_e32 v91, vcc, 0, v143, vcc
	s_mov_b32 s27, 0x48000
	v_pk_fma_f32 v[132:133], v[132:133], s[18:19], v[136:137] op_sel_hi:[1,0,1]
	v_pk_fma_f32 v[120:121], v[120:121], s[18:19], v[136:137] op_sel_hi:[1,0,1]
	v_pk_fma_f32 v[112:113], v[112:113], s[18:19], v[136:137] op_sel_hi:[1,0,1]
	v_pk_fma_f32 v[96:97], v[96:97], s[18:19], v[136:137] op_sel_hi:[1,0,1]
	v_pk_fma_f32 v[88:89], v[88:89], s[18:19], v[136:137] op_sel_hi:[1,0,1]
	v_add_co_u32_e32 v82, vcc, s27, v142
	v_pk_fma_f32 v[80:81], v[80:81], s[18:19], v[136:137] op_sel_hi:[1,0,1]
	v_pk_fma_f32 v[72:73], v[72:73], s[18:19], v[136:137] op_sel_hi:[1,0,1]
	v_pk_fma_f32 v[68:69], v[68:69], s[18:19], v[124:125] op_sel_hi:[1,0,1]
	v_pk_mul_f32 v[132:133], v[132:133], s[20:21] op_sel_hi:[1,0]
	v_pk_mul_f32 v[120:121], v[120:121], s[20:21] op_sel_hi:[1,0]
	v_pk_mul_f32 v[112:113], v[112:113], s[20:21] op_sel_hi:[1,0]
	v_pk_mul_f32 v[96:97], v[96:97], s[20:21] op_sel_hi:[1,0]
	v_pk_mul_f32 v[88:89], v[88:89], s[20:21] op_sel_hi:[1,0]
	v_addc_co_u32_e32 v83, vcc, 0, v143, vcc
	v_pk_mul_f32 v[80:81], v[80:81], s[20:21] op_sel_hi:[1,0]
	s_mov_b32 s27, 0x50000
	v_pk_mul_f32 v[72:73], v[72:73], s[20:21] op_sel_hi:[1,0]
	v_pk_mul_f32 v[68:69], v[68:69], s[20:21] op_sel_hi:[1,0]
	v_cvt_pk_fp8_f32 v156, v132, v133 op_sel:[0,0,1]
	v_cvt_pk_fp8_f32 v128, v120, v121 op_sel:[0,0,1]
	v_cvt_pk_fp8_f32 v116, v112, v113 op_sel:[0,0,1]
	v_cvt_pk_fp8_f32 v100, v96, v97 op_sel:[0,0,1]
	v_cvt_pk_fp8_f32 v92, v88, v89 op_sel:[0,0,1]
	v_cvt_pk_fp8_f32 v84, v80, v81 op_sel:[0,0,1]
	v_add_co_u32_e32 v74, vcc, s27, v142
	v_cvt_pk_fp8_f32 v76, v72, v73 op_sel:[0,0,1]
	v_cvt_pk_fp8_f32 v77, v68, v69 op_sel:[0,0,1]
	v_addc_co_u32_e32 v75, vcc, 0, v143, vcc
	s_mov_b32 s27, 0x58000
	v_add_co_u32_e32 v66, vcc, s27, v142
	global_store_dwordx2 v[142:143], v[156:157], off
	s_nop 0
	v_addc_co_u32_e32 v67, vcc, 0, v143, vcc
	global_store_dwordx2 v[114:115], v[128:129], off
	global_store_dwordx2 v[106:107], v[116:117], off
	global_store_dwordx2 v[90:91], v[100:101], off
	global_store_dwordx2 v[82:83], v[92:93], off
	global_store_dwordx2 v[74:75], v[84:85], off
	global_store_dwordx2 v[66:67], v[76:77], off
	s_waitcnt vmcnt(8)
	v_mov_b32_e32 v66, v160
	v_mov_b32_e32 v67, v161
	v_mov_b32_e32 v68, v162
	v_mov_b32_e32 v69, v163
	v_mov_b32_e32 v70, v164
	v_mov_b32_e32 v71, v165
	v_mov_b32_e32 v72, v166
	v_mov_b32_e32 v73, v167
	v_mov_b32_e32 v77, v139
	v_mov_b32_e32 v76, v139
	v_lshl_add_u64 v[126:127], v[142:143], 0, s[40:41]
	s_mov_b64 s[40:41], 0x10000
	v_lshl_add_u64 v[114:115], v[142:143], 0, s[40:41]
	s_mov_b64 s[40:41], 0x18000
	v_lshl_add_u64 v[106:107], v[142:143], 0, s[40:41]
	s_mov_b64 s[40:41], 0x40000
	v_lshl_add_u64 v[98:99], v[142:143], 0, s[40:41]
	s_mov_b64 s[40:41], 0x48000
	v_lshl_add_u64 v[90:91], v[142:143], 0, s[40:41]
	s_mov_b64 s[40:41], 0x50000
	v_lshl_add_u64 v[82:83], v[142:143], 0, s[40:41]
	s_mov_b64 s[40:41], 0x58000
	v_lshl_add_u64 v[74:75], v[142:143], 0, s[40:41]
	s_mov_b64 s[40:41], -1
	s_and_b64 vcc, exec, s[2:3]
	v_pk_fma_f32 v[58:59], v[58:59], s[18:19], v[66:67] op_sel_hi:[1,0,1]
	s_nop 0
	v_pk_mul_f32 v[58:59], v[58:59], s[20:21] op_sel_hi:[1,0]
	v_pk_fma_f32 v[50:51], v[50:51], s[18:19], v[66:67] op_sel_hi:[1,0,1]
	v_cvt_pk_fp8_f32 v77, v58, v59
	v_pk_mul_f32 v[50:51], v[50:51], s[20:21] op_sel_hi:[1,0]
	v_mov_b32_e32 v59, v139
	v_pk_fma_f32 v[42:43], v[42:43], s[18:19], v[66:67] op_sel_hi:[1,0,1]
	v_cvt_pk_fp8_f32 v59, v50, v51
	v_pk_mul_f32 v[42:43], v[42:43], s[20:21] op_sel_hi:[1,0]
	v_mov_b32_e32 v51, v139
	v_pk_fma_f32 v[34:35], v[34:35], s[18:19], v[66:67] op_sel_hi:[1,0,1]
	v_cvt_pk_fp8_f32 v51, v42, v43
	v_pk_mul_f32 v[34:35], v[34:35], s[20:21] op_sel_hi:[1,0]
	v_mov_b32_e32 v43, v139
	v_pk_fma_f32 v[26:27], v[26:27], s[18:19], v[66:67] op_sel_hi:[1,0,1]
	v_cvt_pk_fp8_f32 v43, v34, v35
	v_pk_mul_f32 v[26:27], v[26:27], s[20:21] op_sel_hi:[1,0]
	v_mov_b32_e32 v35, v139
	v_pk_fma_f32 v[18:19], v[18:19], s[18:19], v[66:67] op_sel_hi:[1,0,1]
	v_cvt_pk_fp8_f32 v35, v26, v27
	v_pk_mul_f32 v[18:19], v[18:19], s[20:21] op_sel_hi:[1,0]
	v_mov_b32_e32 v27, v139
	v_pk_fma_f32 v[10:11], v[10:11], s[18:19], v[66:67] op_sel_hi:[1,0,1]
	v_pk_fma_f32 v[62:63], v[62:63], s[18:19], v[70:71] op_sel_hi:[1,0,1]
	v_pk_fma_f32 v[54:55], v[54:55], s[18:19], v[70:71] op_sel_hi:[1,0,1]
	v_pk_fma_f32 v[46:47], v[46:47], s[18:19], v[70:71] op_sel_hi:[1,0,1]
	v_pk_fma_f32 v[38:39], v[38:39], s[18:19], v[70:71] op_sel_hi:[1,0,1]
; __device__ __forceinline__ int fresh_lane() { int l = (int)__builtin_amdgcn_mbcnt_hi(~0u, __builtin_amdgcn_mbcnt_lo(~0u, 0u)); asm volatile("" : "+v"(l)); return l; }
; __device__ __forceinline__ unsigned pk4_fp8(float a, float b, float c, float d) { int p = 0; p = __builtin_amdgcn_cvt_pk_fp8_f32(a, b, p, false); p = __builtin_amdgcn_cvt_pk_fp8_f32(c, d, p, true); return (unsigned)p; }
; #define PG8_BAR __builtin_amdgcn_s_barrier()
;     __device__ __forceinline__ void operator()(const f32x4 (&acc)[2][2][4][2], const Unit& u, int wr, int wc, int fr, int fq) const {
;         const int row0 = poff[u.e] + u.pm * BM + wr * 64 + fr, col0 = u.pn * BM + wc * 32 + 8 * fq;
;         const float* bp = bias + (size_t)u.e * D + col0;
; #pragma unroll
;         for (int bj = 0; bj < 2; ++bj) { const f32x4 b0 = *(const f32x4*)(bp + bj * HALF), b1 = *(const f32x4*)(bp + bj * HALF + 4);
; #pragma unroll
;             for (int ai = 0; ai < 2; ++ai)
; #pragma unroll
;                 for (int m = 0; m < 4; ++m) { unsigned char* rowp = YS + (size_t)(row0 + ai * HALF + m * 16) * D + col0 + bj * HALF;
;                     const f32x4 v0 = (acc[ai][bj][m][0] * WINV + b0) * YSCALE, v1 = (acc[ai][bj][m][1] * WINV + b1) * YSCALE;
;                     u32x2 w; w.x = pk4_fp8(v0[0], v0[1], v0[2], v0[3]); w.y = pk4_fp8(v1[0], v1[1], v1[2], v1[3]);
;                     *(u32x2*)rowp = w; } }
; template <class Epi, class Sched>
; __device__ __forceinline__ void gemm_phase(LAS unsigned char* lds, const Sched& S, const Epi& E) {
;     ...
;         if (wr == 0) PG8_BAR;
;         { const int l2 = fresh_lane(); E(acc, cur, wr, wc, l2 & 15, l2 >> 4); }
;         if (!has_next) break;
; #pragma unroll
;         for (int a = 0; a < 2; ++a)
; #pragma unroll
;             for (int b = 0; b < 2; ++b)
; #pragma unroll
;                 for (int m = 0; m < 4; ++m)
; #pragma unroll
;                     for (int n = 0; n < 2; ++n) acc[a][b][m][n] = (f32x4){0.f, 0.f, 0.f, 0.f};
;         cur = nxt; cA = nA; cB = nB; ++ui;
;         if (wr == 1) PG8_BAR;
;     }
	v_pk_fma_f32 v[30:31], v[30:31], s[18:19], v[70:71] op_sel_hi:[1,0,1]
	v_pk_fma_f32 v[22:23], v[22:23], s[18:19], v[70:71] op_sel_hi:[1,0,1]
	v_cvt_pk_fp8_f32 v27, v18, v19
	v_pk_fma_f32 v[14:15], v[14:15], s[18:19], v[70:71] op_sel_hi:[1,0,1]
	v_pk_mul_f32 v[10:11], v[10:11], s[20:21] op_sel_hi:[1,0]
	v_mov_b32_e32 v19, v139
	v_pk_fma_f32 v[6:7], v[6:7], s[18:19], v[70:71] op_sel_hi:[1,0,1]
	v_pk_fma_f32 v[2:3], v[2:3], s[18:19], v[66:67] op_sel_hi:[1,0,1]
	v_pk_mul_f32 v[62:63], v[62:63], s[20:21] op_sel_hi:[1,0]
	v_pk_mul_f32 v[54:55], v[54:55], s[20:21] op_sel_hi:[1,0]
	v_mov_b32_e32 v58, v139
	v_pk_mul_f32 v[46:47], v[46:47], s[20:21] op_sel_hi:[1,0]
	v_mov_b32_e32 v50, v139
	v_pk_mul_f32 v[38:39], v[38:39], s[20:21] op_sel_hi:[1,0]
	v_mov_b32_e32 v42, v139
	v_pk_mul_f32 v[30:31], v[30:31], s[20:21] op_sel_hi:[1,0]
	v_mov_b32_e32 v34, v139
	v_pk_mul_f32 v[22:23], v[22:23], s[20:21] op_sel_hi:[1,0]
	v_mov_b32_e32 v26, v139
	v_pk_mul_f32 v[14:15], v[14:15], s[20:21] op_sel_hi:[1,0]
	v_mov_b32_e32 v18, v139
	v_cvt_pk_fp8_f32 v19, v10, v11
	v_pk_mul_f32 v[6:7], v[6:7], s[20:21] op_sel_hi:[1,0]
	v_pk_mul_f32 v[2:3], v[2:3], s[20:21] op_sel_hi:[1,0]
	v_mov_b32_e32 v10, v139
	v_mov_b32_e32 v11, v139
	v_cvt_pk_fp8_f32 v76, v62, v63
	v_cvt_pk_fp8_f32 v58, v54, v55
	v_cvt_pk_fp8_f32 v50, v46, v47
	v_cvt_pk_fp8_f32 v42, v38, v39
	v_cvt_pk_fp8_f32 v34, v30, v31
	v_cvt_pk_fp8_f32 v26, v22, v23
	v_cvt_pk_fp8_f32 v18, v14, v15
	v_cvt_pk_fp8_f32 v10, v6, v7
	v_cvt_pk_fp8_f32 v11, v2, v3
	v_pk_fma_f32 v[64:65], v[64:65], s[18:19], v[72:73] op_sel_hi:[1,0,1]
	v_pk_fma_f32 v[60:61], v[60:61], s[18:19], v[68:69] op_sel_hi:[1,0,1]
	v_pk_fma_f32 v[56:57], v[56:57], s[18:19], v[72:73] op_sel_hi:[1,0,1]
	v_pk_fma_f32 v[52:53], v[52:53], s[18:19], v[68:69] op_sel_hi:[1,0,1]
	v_pk_fma_f32 v[48:49], v[48:49], s[18:19], v[72:73] op_sel_hi:[1,0,1]
	v_pk_fma_f32 v[44:45], v[44:45], s[18:19], v[68:69] op_sel_hi:[1,0,1]
	v_pk_fma_f32 v[40:41], v[40:41], s[18:19], v[72:73] op_sel_hi:[1,0,1]
	v_pk_fma_f32 v[36:37], v[36:37], s[18:19], v[68:69] op_sel_hi:[1,0,1]
	v_pk_fma_f32 v[32:33], v[32:33], s[18:19], v[72:73] op_sel_hi:[1,0,1]
	v_pk_fma_f32 v[28:29], v[28:29], s[18:19], v[68:69] op_sel_hi:[1,0,1]
	v_pk_fma_f32 v[24:25], v[24:25], s[18:19], v[72:73] op_sel_hi:[1,0,1]
	v_pk_fma_f32 v[20:21], v[20:21], s[18:19], v[68:69] op_sel_hi:[1,0,1]
	v_pk_fma_f32 v[16:17], v[16:17], s[18:19], v[72:73] op_sel_hi:[1,0,1]
	v_pk_fma_f32 v[12:13], v[12:13], s[18:19], v[68:69] op_sel_hi:[1,0,1]
	v_pk_fma_f32 v[8:9], v[8:9], s[18:19], v[72:73] op_sel_hi:[1,0,1]
	v_pk_fma_f32 v[4:5], v[4:5], s[18:19], v[68:69] op_sel_hi:[1,0,1]
	v_pk_mul_f32 v[64:65], v[64:65], s[20:21] op_sel_hi:[1,0]
	v_pk_mul_f32 v[60:61], v[60:61], s[20:21] op_sel_hi:[1,0]
	v_pk_mul_f32 v[56:57], v[56:57], s[20:21] op_sel_hi:[1,0]
	v_pk_mul_f32 v[52:53], v[52:53], s[20:21] op_sel_hi:[1,0]
	v_pk_mul_f32 v[48:49], v[48:49], s[20:21] op_sel_hi:[1,0]
	v_pk_mul_f32 v[44:45], v[44:45], s[20:21] op_sel_hi:[1,0]
	v_pk_mul_f32 v[40:41], v[40:41], s[20:21] op_sel_hi:[1,0]
	v_pk_mul_f32 v[36:37], v[36:37], s[20:21] op_sel_hi:[1,0]
	v_pk_mul_f32 v[32:33], v[32:33], s[20:21] op_sel_hi:[1,0]
	v_pk_mul_f32 v[28:29], v[28:29], s[20:21] op_sel_hi:[1,0]
	v_pk_mul_f32 v[24:25], v[24:25], s[20:21] op_sel_hi:[1,0]
	v_pk_mul_f32 v[20:21], v[20:21], s[20:21] op_sel_hi:[1,0]
	v_pk_mul_f32 v[16:17], v[16:17], s[20:21] op_sel_hi:[1,0]
	v_pk_mul_f32 v[12:13], v[12:13], s[20:21] op_sel_hi:[1,0]
	v_pk_mul_f32 v[8:9], v[8:9], s[20:21] op_sel_hi:[1,0]
	v_pk_mul_f32 v[4:5], v[4:5], s[20:21] op_sel_hi:[1,0]
	v_cvt_pk_fp8_f32 v76, v64, v65 op_sel:[0,0,1]
	v_cvt_pk_fp8_f32 v77, v60, v61 op_sel:[0,0,1]
	v_cvt_pk_fp8_f32 v58, v56, v57 op_sel:[0,0,1]
	v_cvt_pk_fp8_f32 v59, v52, v53 op_sel:[0,0,1]
	v_cvt_pk_fp8_f32 v50, v48, v49 op_sel:[0,0,1]
	v_cvt_pk_fp8_f32 v51, v44, v45 op_sel:[0,0,1]
	v_cvt_pk_fp8_f32 v42, v40, v41 op_sel:[0,0,1]
	v_cvt_pk_fp8_f32 v43, v36, v37 op_sel:[0,0,1]
	v_cvt_pk_fp8_f32 v34, v32, v33 op_sel:[0,0,1]
	v_cvt_pk_fp8_f32 v35, v28, v29 op_sel:[0,0,1]
	v_cvt_pk_fp8_f32 v26, v24, v25 op_sel:[0,0,1]
	v_cvt_pk_fp8_f32 v27, v20, v21 op_sel:[0,0,1]
	v_cvt_pk_fp8_f32 v18, v16, v17 op_sel:[0,0,1]
	v_cvt_pk_fp8_f32 v19, v12, v13 op_sel:[0,0,1]
	v_cvt_pk_fp8_f32 v10, v8, v9 op_sel:[0,0,1]
	v_cvt_pk_fp8_f32 v11, v4, v5 op_sel:[0,0,1]
	global_store_dwordx2 v[142:143], v[76:77], off offset:128
	global_store_dwordx2 v[126:127], v[58:59], off offset:128
	global_store_dwordx2 v[114:115], v[50:51], off offset:128
	global_store_dwordx2 v[106:107], v[42:43], off offset:128
	global_store_dwordx2 v[98:99], v[34:35], off offset:128
	global_store_dwordx2 v[90:91], v[26:27], off offset:128
	global_store_dwordx2 v[82:83], v[18:19], off offset:128
	global_store_dwordx2 v[74:75], v[10:11], off offset:128
	s_cbranch_vccnz .LBB0_1455
	s_andn2_b64 vcc, exec, s[0:1]
	s_cbranch_vccnz .LBB0_1454
	s_barrier
	s_branch .LBB0_1454
